# both MoE GEMM K-loops at 16 MFMAs per interval plus MoE gate/up on 230 workgroups and 26 workgroups on the down-weight conversion (was 232/24)
# speedup vs baseline: 1.0281x; 1.0278x over previous
; #define LAS __attribute__((address_space(3)))
; __device__ __forceinline__ void moe_weight_convert(const Params& p, Frame& F, int gw, int NGW, int it0, int NIT) {
;     LAS unsigned char* tile = F.lds + 16384 + F.wave * 8192;
;     const int lane = F.lane, kq = lane >> 4, nq = lane & 15;
;     __syncthreads();
;     for (int i = F.tid; i < DM; i += 512) { *(LAS float*)(F.lds + 4 * i) = p.in[11][i] * 64.0f; *(LAS float*)(F.lds + 8192 + 4 * i) = 64.0f; }
;     __syncthreads();
; __global__ void __launch_bounds__(512, 2) hymba_fwd(Params p) {
;     ...
;         const int ngm = (F.G == 256) ? NG_MOE1 : F.G;
;         if (ngm == F.G) { moe_weight_convert(p, F, (int)blockIdx.x * 8 + F.wave, F.G * 8, CONV_N_GU, CONV_N_ALL); __syncthreads(); }
;         if ((int)blockIdx.x < ngm) {
;         moe_tables(p, F);
;         pg8::Gemm g{(const bf16_t*)(ws + WS_X1B), (const bf16_t*)(ws + WS_WGU), DM / 2};
;         pg8::MoeOrder S; S.init((const LAS int*)(F.lds + L_TILE0), (const LAS int*)(F.lds + L_CNT), (const int*)(ws + WS_LTOK), 16, ngm, (int)blockIdx.x);
;         EpiMoe1 E{(unsigned char*)(ws + WS_ACT), p.in[15], p.in[17], (const float*)(ws + WS_LRS), (const LAS int*)(F.lds + L_CNT)};
;         pg8::gemm_phase<EpiMoe1, pg8::MoeOrder, true, true, false, true>(ring, g, S, E);
;         } else moe_weight_convert(p, F, ((int)blockIdx.x - ngm) * 8 + F.wave, (F.G - ngm) * 8, CONV_N_GU, CONV_N_ALL);
.LBB0_875:
	s_and_b64 s[0:1], exec, s[0:1]
	s_cselect_b32 s34, 0xe6, s94
	v_readlane_b32 s0, v245, 18
	s_cmp_ge_i32 s0, s34
	s_mov_b64 s[0:1], -1
	s_cbranch_scc0 .LBB0_915
	v_readlane_b32 s0, v245, 39
	s_waitcnt vmcnt(0)
	v_lshlrev_b32_e32 v4, 2, v0
	v_mov_b32_e32 v5, 0
	v_readlane_b32 s1, v245, 40
	v_readlane_b32 s2, v245, 41
	v_readlane_b32 s3, v245, 42
	v_readlane_b32 s4, v245, 43
	v_readlane_b32 s6, v245, 45
	v_readlane_b32 s7, v245, 46
	v_or_b32_e32 v1, 0xfffffe00, v0
	s_mov_b64 s[0:1], 0
	v_lshl_add_u64 v[2:3], s[6:7], 0, v[4:5]
	v_add_u32_e32 v4, 0, v4
	v_mov_b32_e32 v5, 0x42800000
	s_mov_b64 s[2:3], 0x800
	s_movk_i32 s4, 0x5ff
	s_waitcnt lgkmcnt(0)
	s_barrier
	v_readlane_b32 s5, v245, 44
	v_readlane_b32 s8, v245, 47
	v_readlane_b32 s9, v245, 48
	v_readlane_b32 s10, v245, 49
	v_readlane_b32 s11, v245, 50
	v_readlane_b32 s12, v245, 51
	v_readlane_b32 s13, v245, 52
	v_readlane_b32 s14, v245, 53
	v_readlane_b32 s15, v245, 54
